# merge GEMM final epilogue: the 16 gate-tile loads issued together (two bases + immediate offsets, into fragment registers dead after the K loop) behind counted waits instead of one load per wait
# baseline (speedup 1.0000x reference)
.LBB0_1529:
	v_mov_b32_e32 v134, v143
	v_mov_b32_e32 v135, v142
	s_lshl_b32 s6, s63, 3
	s_add_i32 s6, s6, s64
	v_lshlrev_b32_e32 v130, 4, v135
	s_addk_i32 s6, 0x630
	v_add3_u32 v130, v134, s57, v130
	s_ashr_i32 s7, s6, 31
	v_ashrrev_i32_e32 v131, 31, v130
	s_lshl_b64 s[6:7], s[6:7], 16
	v_lshl_add_u64 v[132:133], v[130:131], 3, s[14:15]
	v_lshl_add_u64 v[132:133], v[132:133], 0, s[6:7]
	global_load_dwordx2 v[136:137], v[132:133], off
	s_mov_b64 s[98:99], 0x1000
	v_lshl_add_u64 v[190:191], v[132:133], 0, s[98:99]
	global_load_dwordx2 v[160:161], v[132:133], off offset:512
	global_load_dwordx2 v[162:163], v[132:133], off offset:1024
	global_load_dwordx2 v[164:165], v[132:133], off offset:1536
	global_load_dwordx2 v[166:167], v[132:133], off offset:2048
	global_load_dwordx2 v[168:169], v[132:133], off offset:2560
	global_load_dwordx2 v[170:171], v[132:133], off offset:3072
	global_load_dwordx2 v[172:173], v[132:133], off offset:3584
	global_load_dwordx2 v[174:175], v[190:191], off
	global_load_dwordx2 v[176:177], v[190:191], off offset:512
	global_load_dwordx2 v[178:179], v[190:191], off offset:1024
	global_load_dwordx2 v[180:181], v[190:191], off offset:1536
	global_load_dwordx2 v[182:183], v[190:191], off offset:2048
	global_load_dwordx2 v[184:185], v[190:191], off offset:2560
	global_load_dwordx2 v[186:187], v[190:191], off offset:3072
	global_load_dwordx2 v[188:189], v[190:191], off offset:3584
	s_lshl_b32 s26, s63, 8
	s_lshl_b32 s27, s64, 8
	s_add_i32 s26, s26, s54
	s_or_b32 s27, s27, s55
	v_add_u32_e32 v134, s26, v134
	v_lshl_add_u32 v132, v135, 3, s27
	v_ashrrev_i32_e32 v135, 31, v134
	v_lshlrev_b64 v[152:153], 11, v[134:135]
	v_mov_b32_e32 v150, 0
	v_mov_b32_e32 v151, 0
	v_add_u32_e32 v154, 64, v130
	v_ashrrev_i32_e32 v133, 31, v132
	v_lshl_add_u64 v[152:153], s[18:19], 0, v[152:153]
	v_ashrrev_i32_e32 v155, 31, v154
	s_andn2_b64 vcc, exec, s[24:25]
	s_waitcnt vmcnt(15)
	v_cvt_f32_ubyte0_e32 v131, v136
	v_cvt_f32_ubyte0_e32 v135, v137
	v_cvt_f32_ubyte1_e32 v149, v136
	v_cvt_f32_ubyte1_e32 v156, v137
	v_mul_f32_e32 v131, v141, v131
	v_mul_f32_e32 v135, v141, v135
	v_mul_f32_e32 v149, v141, v149
	v_mul_f32_e32 v156, v141, v156
	v_mul_f32_e32 v126, v126, v131
	v_mul_f32_e32 v127, v127, v149
	v_mul_f32_e32 v122, v122, v135
	v_mul_f32_e32 v123, v123, v156
	v_cvt_pk_fp8_f32 v150, v126, v127
	v_cvt_pk_fp8_f32 v151, v122, v123
	v_cvt_f32_ubyte2_e32 v157, v136
	v_cvt_f32_ubyte2_e32 v158, v137
	v_cvt_f32_ubyte3_e32 v136, v136
	v_cvt_f32_ubyte3_e32 v137, v137
	v_mul_f32_e32 v157, v141, v157
	v_mul_f32_e32 v158, v141, v158
	v_mul_f32_e32 v136, v141, v136
	v_mul_f32_e32 v137, v141, v137
	v_mul_f32_e32 v128, v128, v157
	v_mul_f32_e32 v129, v129, v136
	v_mul_f32_e32 v122, v124, v158
	v_mul_f32_e32 v123, v125, v137
	v_cvt_pk_fp8_f32 v150, v128, v129 op_sel:[0,0,1]
	v_cvt_pk_fp8_f32 v151, v122, v123 op_sel:[0,0,1]
	v_lshl_add_u64 v[122:123], v[152:153], 0, v[132:133]
	v_lshl_add_u64 v[124:125], v[154:155], 3, s[14:15]
	v_lshl_add_u64 v[124:125], v[124:125], 0, s[6:7]
	global_store_dwordx2 v[122:123], v[150:151], off
	v_mov_b32_e32 v126, 0
	v_mov_b32_e32 v127, 0
	v_add_u32_e32 v128, 0x80, v130
	s_waitcnt vmcnt(15)
	v_cvt_f32_ubyte0_e32 v129, v160
	v_cvt_f32_ubyte0_e32 v131, v161
	v_cvt_f32_ubyte1_e32 v135, v160
	v_cvt_f32_ubyte1_e32 v136, v161
	v_mul_f32_e32 v129, v141, v129
	v_mul_f32_e32 v131, v141, v131
	v_mul_f32_e32 v135, v141, v135
	v_mul_f32_e32 v136, v141, v136
	v_mul_f32_e32 v118, v118, v129
	v_mul_f32_e32 v119, v119, v135
	v_mul_f32_e32 v114, v114, v131
	v_mul_f32_e32 v115, v115, v136
	v_cvt_pk_fp8_f32 v126, v118, v119
	v_cvt_pk_fp8_f32 v127, v114, v115
	v_cvt_f32_ubyte2_e32 v137, v160
	v_cvt_f32_ubyte2_e32 v149, v161
	v_cvt_f32_ubyte3_e32 v124, v160
	v_cvt_f32_ubyte3_e32 v125, v161
	v_mul_f32_e32 v137, v141, v137
	v_mul_f32_e32 v149, v141, v149
	v_mul_f32_e32 v124, v141, v124
	v_mul_f32_e32 v125, v141, v125
	v_mul_f32_e32 v120, v120, v137
	v_mul_f32_e32 v121, v121, v124
	v_mul_f32_e32 v114, v116, v149
	v_mul_f32_e32 v115, v117, v125
	v_cvt_pk_fp8_f32 v126, v120, v121 op_sel:[0,0,1]
	v_cvt_pk_fp8_f32 v127, v114, v115 op_sel:[0,0,1]
	v_ashrrev_i32_e32 v129, 31, v128
	v_lshl_add_u64 v[114:115], v[128:129], 3, s[14:15]
	v_lshl_add_u64 v[114:115], v[114:115], 0, s[6:7]
	global_store_dwordx2 v[122:123], v[126:127], off offset:128
	v_mov_b32_e32 v116, 0
	v_mov_b32_e32 v117, 0
	v_add_u32_e32 v118, 16, v134
	v_ashrrev_i32_e32 v119, 31, v118
	v_add_u32_e32 v120, 0xc0, v130
	v_lshlrev_b64 v[118:119], 11, v[118:119]
	v_ashrrev_i32_e32 v121, 31, v120
	v_lshl_add_u64 v[118:119], s[18:19], 0, v[118:119]
	s_waitcnt vmcnt(15)
	v_cvt_f32_ubyte0_e32 v122, v162
	v_cvt_f32_ubyte0_e32 v123, v163
	v_cvt_f32_ubyte1_e32 v124, v162
	v_cvt_f32_ubyte1_e32 v125, v163
	v_mul_f32_e32 v122, v141, v122
	v_mul_f32_e32 v123, v141, v123
	v_mul_f32_e32 v124, v141, v124
	v_mul_f32_e32 v125, v141, v125
	v_mul_f32_e32 v110, v110, v122
	v_mul_f32_e32 v111, v111, v124
	v_mul_f32_e32 v106, v106, v123
	v_mul_f32_e32 v107, v107, v125
	v_cvt_pk_fp8_f32 v116, v110, v111
	v_cvt_pk_fp8_f32 v117, v106, v107
	v_cvt_f32_ubyte2_e32 v126, v162
	v_cvt_f32_ubyte2_e32 v127, v163
	v_cvt_f32_ubyte3_e32 v114, v162
	v_cvt_f32_ubyte3_e32 v115, v163
	v_mul_f32_e32 v126, v141, v126
	v_mul_f32_e32 v127, v141, v127
	v_mul_f32_e32 v114, v141, v114
	v_mul_f32_e32 v115, v141, v115
	v_mul_f32_e32 v112, v112, v126
	v_mul_f32_e32 v113, v113, v114
	v_mul_f32_e32 v106, v108, v127
	v_mul_f32_e32 v107, v109, v115
	v_cvt_pk_fp8_f32 v116, v112, v113 op_sel:[0,0,1]
	v_cvt_pk_fp8_f32 v117, v106, v107 op_sel:[0,0,1]
	v_lshl_add_u64 v[106:107], v[120:121], 3, s[14:15]
	v_lshl_add_u64 v[108:109], v[118:119], 0, v[132:133]
	v_lshl_add_u64 v[106:107], v[106:107], 0, s[6:7]
	global_store_dwordx2 v[108:109], v[116:117], off
	v_mov_b32_e32 v110, 0
	v_mov_b32_e32 v111, 0
	v_add_u32_e32 v112, 0x100, v130
	s_waitcnt vmcnt(15)
	v_cvt_f32_ubyte0_e32 v113, v164
	v_cvt_f32_ubyte0_e32 v114, v165
	v_cvt_f32_ubyte1_e32 v115, v164
	v_cvt_f32_ubyte1_e32 v116, v165
	v_mul_f32_e32 v113, v141, v113
	v_mul_f32_e32 v114, v141, v114
	v_mul_f32_e32 v115, v141, v115
	v_mul_f32_e32 v116, v141, v116
	v_mul_f32_e32 v102, v102, v113
	v_mul_f32_e32 v103, v103, v115
	v_mul_f32_e32 v98, v98, v114
	v_mul_f32_e32 v99, v99, v116
	v_cvt_pk_fp8_f32 v110, v102, v103
	v_cvt_pk_fp8_f32 v111, v98, v99
	v_cvt_f32_ubyte2_e32 v117, v164
	v_cvt_f32_ubyte2_e32 v118, v165
	v_cvt_f32_ubyte3_e32 v106, v164
	v_cvt_f32_ubyte3_e32 v107, v165
	v_mul_f32_e32 v117, v141, v117
	v_mul_f32_e32 v118, v141, v118
	v_mul_f32_e32 v106, v141, v106
	v_mul_f32_e32 v107, v141, v107
	v_mul_f32_e32 v104, v104, v117
	v_mul_f32_e32 v105, v105, v106
	v_mul_f32_e32 v98, v100, v118
	v_mul_f32_e32 v99, v101, v107
	v_cvt_pk_fp8_f32 v110, v104, v105 op_sel:[0,0,1]
	v_cvt_pk_fp8_f32 v111, v98, v99 op_sel:[0,0,1]
	v_ashrrev_i32_e32 v113, 31, v112
	v_lshl_add_u64 v[98:99], v[112:113], 3, s[14:15]
	v_lshl_add_u64 v[98:99], v[98:99], 0, s[6:7]
	global_store_dwordx2 v[108:109], v[110:111], off offset:128
	v_mov_b32_e32 v100, 0
	v_mov_b32_e32 v101, 0
	v_add_u32_e32 v102, 32, v134
	v_ashrrev_i32_e32 v103, 31, v102
	v_add_u32_e32 v104, 0x140, v130
	v_lshlrev_b64 v[102:103], 11, v[102:103]
	v_ashrrev_i32_e32 v105, 31, v104
	v_lshl_add_u64 v[102:103], s[18:19], 0, v[102:103]
	s_waitcnt vmcnt(15)
	v_cvt_f32_ubyte0_e32 v106, v166
	v_cvt_f32_ubyte0_e32 v107, v167
	v_cvt_f32_ubyte1_e32 v108, v166
	v_cvt_f32_ubyte1_e32 v109, v167
	v_mul_f32_e32 v106, v141, v106
	v_mul_f32_e32 v107, v141, v107
	v_mul_f32_e32 v108, v141, v108
	v_mul_f32_e32 v109, v141, v109
	v_mul_f32_e32 v94, v94, v106
	v_mul_f32_e32 v95, v95, v108
	v_mul_f32_e32 v90, v90, v107
	v_mul_f32_e32 v91, v91, v109
	v_cvt_pk_fp8_f32 v100, v94, v95
	v_cvt_pk_fp8_f32 v101, v90, v91
	v_cvt_f32_ubyte2_e32 v110, v166
	v_cvt_f32_ubyte2_e32 v111, v167
	v_cvt_f32_ubyte3_e32 v98, v166
	v_cvt_f32_ubyte3_e32 v99, v167
	v_mul_f32_e32 v110, v141, v110
	v_mul_f32_e32 v111, v141, v111
	v_mul_f32_e32 v98, v141, v98
	v_mul_f32_e32 v99, v141, v99
	v_mul_f32_e32 v96, v96, v110
	v_mul_f32_e32 v97, v97, v98
	v_mul_f32_e32 v90, v92, v111
	v_mul_f32_e32 v91, v93, v99
	v_cvt_pk_fp8_f32 v100, v96, v97 op_sel:[0,0,1]
	v_cvt_pk_fp8_f32 v101, v90, v91 op_sel:[0,0,1]
	v_lshl_add_u64 v[90:91], v[104:105], 3, s[14:15]
	v_lshl_add_u64 v[92:93], v[102:103], 0, v[132:133]
	v_lshl_add_u64 v[90:91], v[90:91], 0, s[6:7]
	global_store_dwordx2 v[92:93], v[100:101], off
	v_mov_b32_e32 v94, 0
	v_mov_b32_e32 v95, 0
	v_add_u32_e32 v96, 0x180, v130
	s_waitcnt vmcnt(15)
	v_cvt_f32_ubyte0_e32 v97, v168
	v_cvt_f32_ubyte0_e32 v98, v169
	v_cvt_f32_ubyte1_e32 v99, v168
	v_cvt_f32_ubyte1_e32 v100, v169
	v_mul_f32_e32 v97, v141, v97
	v_mul_f32_e32 v98, v141, v98
	v_mul_f32_e32 v99, v141, v99
	v_mul_f32_e32 v100, v141, v100
	v_mul_f32_e32 v86, v86, v97
	v_mul_f32_e32 v87, v87, v99
	v_mul_f32_e32 v82, v82, v98
	v_mul_f32_e32 v83, v83, v100
	v_cvt_pk_fp8_f32 v94, v86, v87
	v_cvt_pk_fp8_f32 v95, v82, v83
	v_cvt_f32_ubyte2_e32 v101, v168
	v_cvt_f32_ubyte2_e32 v102, v169
	v_cvt_f32_ubyte3_e32 v90, v168
	v_cvt_f32_ubyte3_e32 v91, v169
	v_mul_f32_e32 v101, v141, v101
	v_mul_f32_e32 v102, v141, v102
	v_mul_f32_e32 v90, v141, v90
	v_mul_f32_e32 v91, v141, v91
	v_mul_f32_e32 v88, v88, v101
	v_mul_f32_e32 v89, v89, v90
	v_mul_f32_e32 v82, v84, v102
	v_mul_f32_e32 v83, v85, v91
	v_cvt_pk_fp8_f32 v94, v88, v89 op_sel:[0,0,1]
	v_cvt_pk_fp8_f32 v95, v82, v83 op_sel:[0,0,1]
	v_ashrrev_i32_e32 v97, 31, v96
	v_lshl_add_u64 v[82:83], v[96:97], 3, s[14:15]
	v_lshl_add_u64 v[82:83], v[82:83], 0, s[6:7]
	global_store_dwordx2 v[92:93], v[94:95], off offset:128
	v_mov_b32_e32 v84, 0
	v_mov_b32_e32 v85, 0
	v_add_u32_e32 v86, 48, v134
	v_ashrrev_i32_e32 v87, 31, v86
	v_add_u32_e32 v88, 0x1c0, v130
	v_lshlrev_b64 v[86:87], 11, v[86:87]
	v_ashrrev_i32_e32 v89, 31, v88
	v_lshl_add_u64 v[86:87], s[18:19], 0, v[86:87]
	s_waitcnt vmcnt(15)
	v_cvt_f32_ubyte0_e32 v90, v170
	v_cvt_f32_ubyte0_e32 v91, v171
	v_cvt_f32_ubyte1_e32 v92, v170
	v_cvt_f32_ubyte1_e32 v93, v171
	v_mul_f32_e32 v90, v141, v90
	v_mul_f32_e32 v91, v141, v91
	v_mul_f32_e32 v92, v141, v92
	v_mul_f32_e32 v93, v141, v93
	v_mul_f32_e32 v78, v78, v90
	v_mul_f32_e32 v79, v79, v92
	v_mul_f32_e32 v74, v74, v91
	v_mul_f32_e32 v75, v75, v93
	v_cvt_pk_fp8_f32 v84, v78, v79
	v_cvt_pk_fp8_f32 v85, v74, v75
	v_cvt_f32_ubyte2_e32 v94, v170
	v_cvt_f32_ubyte2_e32 v95, v171
	v_cvt_f32_ubyte3_e32 v82, v170
	v_cvt_f32_ubyte3_e32 v83, v171
	v_mul_f32_e32 v94, v141, v94
	v_mul_f32_e32 v95, v141, v95
	v_mul_f32_e32 v82, v141, v82
	v_mul_f32_e32 v83, v141, v83
	v_mul_f32_e32 v80, v80, v94
	v_mul_f32_e32 v81, v81, v82
	v_mul_f32_e32 v74, v76, v95
	v_mul_f32_e32 v75, v77, v83
	v_cvt_pk_fp8_f32 v84, v80, v81 op_sel:[0,0,1]
	v_cvt_pk_fp8_f32 v85, v74, v75 op_sel:[0,0,1]
	v_lshl_add_u64 v[74:75], v[88:89], 3, s[14:15]
	v_lshl_add_u64 v[76:77], v[86:87], 0, v[132:133]
	v_lshl_add_u64 v[74:75], v[74:75], 0, s[6:7]
	global_store_dwordx2 v[76:77], v[84:85], off
	v_mov_b32_e32 v78, 0
	v_mov_b32_e32 v79, 0
	v_add_u32_e32 v80, 0x200, v130
	s_waitcnt vmcnt(15)
	v_cvt_f32_ubyte0_e32 v81, v172
	v_cvt_f32_ubyte0_e32 v82, v173
	v_cvt_f32_ubyte1_e32 v83, v172
	v_cvt_f32_ubyte1_e32 v84, v173
	v_mul_f32_e32 v81, v141, v81
	v_mul_f32_e32 v82, v141, v82
	v_mul_f32_e32 v83, v141, v83
	v_mul_f32_e32 v84, v141, v84
	v_mul_f32_e32 v70, v70, v81
	v_mul_f32_e32 v71, v71, v83
	v_mul_f32_e32 v66, v66, v82
	v_mul_f32_e32 v67, v67, v84
	v_cvt_pk_fp8_f32 v78, v70, v71
	v_cvt_pk_fp8_f32 v79, v66, v67
	v_cvt_f32_ubyte2_e32 v85, v172
	v_cvt_f32_ubyte2_e32 v86, v173
	v_cvt_f32_ubyte3_e32 v74, v172
	v_cvt_f32_ubyte3_e32 v75, v173
	v_mul_f32_e32 v85, v141, v85
	v_mul_f32_e32 v86, v141, v86
	v_mul_f32_e32 v74, v141, v74
	v_mul_f32_e32 v75, v141, v75
	v_mul_f32_e32 v72, v72, v85
	v_mul_f32_e32 v73, v73, v74
	v_mul_f32_e32 v66, v68, v86
	v_mul_f32_e32 v67, v69, v75
	v_cvt_pk_fp8_f32 v78, v72, v73 op_sel:[0,0,1]
	v_cvt_pk_fp8_f32 v79, v66, v67 op_sel:[0,0,1]
	v_ashrrev_i32_e32 v81, 31, v80
	v_lshl_add_u64 v[66:67], v[80:81], 3, s[14:15]
	v_lshl_add_u64 v[66:67], v[66:67], 0, s[6:7]
	global_store_dwordx2 v[76:77], v[78:79], off offset:128
	v_mov_b32_e32 v68, 0
	v_mov_b32_e32 v69, 0
	v_add_u32_e32 v70, 0x80, v134
	v_ashrrev_i32_e32 v71, 31, v70
	v_add_u32_e32 v72, 0x240, v130
	v_lshlrev_b64 v[70:71], 11, v[70:71]
	v_ashrrev_i32_e32 v73, 31, v72
	v_lshl_add_u64 v[70:71], s[18:19], 0, v[70:71]
	s_waitcnt vmcnt(15)
	v_cvt_f32_ubyte0_e32 v74, v174
	v_cvt_f32_ubyte0_e32 v75, v175
	v_cvt_f32_ubyte1_e32 v76, v174
	v_cvt_f32_ubyte1_e32 v77, v175
	v_mul_f32_e32 v74, v141, v74
	v_mul_f32_e32 v75, v141, v75
	v_mul_f32_e32 v76, v141, v76
	v_mul_f32_e32 v77, v141, v77
	v_mul_f32_e32 v62, v62, v74
	v_mul_f32_e32 v63, v63, v76
	v_mul_f32_e32 v58, v58, v75
	v_mul_f32_e32 v59, v59, v77
	v_cvt_pk_fp8_f32 v68, v62, v63
	v_cvt_pk_fp8_f32 v69, v58, v59
	v_cvt_f32_ubyte2_e32 v78, v174
	v_cvt_f32_ubyte2_e32 v79, v175
	v_cvt_f32_ubyte3_e32 v66, v174
	v_cvt_f32_ubyte3_e32 v67, v175
	v_mul_f32_e32 v78, v141, v78
	v_mul_f32_e32 v79, v141, v79
	v_mul_f32_e32 v66, v141, v66
	v_mul_f32_e32 v67, v141, v67
	v_mul_f32_e32 v64, v64, v78
	v_mul_f32_e32 v65, v65, v66
	v_mul_f32_e32 v58, v60, v79
	v_mul_f32_e32 v59, v61, v67
	v_cvt_pk_fp8_f32 v68, v64, v65 op_sel:[0,0,1]
	v_cvt_pk_fp8_f32 v69, v58, v59 op_sel:[0,0,1]
	v_lshl_add_u64 v[58:59], v[72:73], 3, s[14:15]
	v_lshl_add_u64 v[60:61], v[70:71], 0, v[132:133]
	v_lshl_add_u64 v[58:59], v[58:59], 0, s[6:7]
	global_store_dwordx2 v[60:61], v[68:69], off
	v_mov_b32_e32 v62, 0
	v_mov_b32_e32 v63, 0
	v_add_u32_e32 v64, 0x280, v130
	s_waitcnt vmcnt(15)
	v_cvt_f32_ubyte0_e32 v65, v176
	v_cvt_f32_ubyte0_e32 v66, v177
	v_cvt_f32_ubyte1_e32 v67, v176
	v_cvt_f32_ubyte1_e32 v68, v177
	v_mul_f32_e32 v65, v141, v65
	v_mul_f32_e32 v66, v141, v66
	v_mul_f32_e32 v67, v141, v67
	v_mul_f32_e32 v68, v141, v68
	v_mul_f32_e32 v54, v54, v65
	v_mul_f32_e32 v55, v55, v67
	v_mul_f32_e32 v50, v50, v66
	v_mul_f32_e32 v51, v51, v68
	v_cvt_pk_fp8_f32 v62, v54, v55
	v_cvt_pk_fp8_f32 v63, v50, v51
	v_cvt_f32_ubyte2_e32 v69, v176
	v_cvt_f32_ubyte2_e32 v70, v177
	v_cvt_f32_ubyte3_e32 v58, v176
	v_cvt_f32_ubyte3_e32 v59, v177
	v_mul_f32_e32 v69, v141, v69
	v_mul_f32_e32 v70, v141, v70
	v_mul_f32_e32 v58, v141, v58
	v_mul_f32_e32 v59, v141, v59
	v_mul_f32_e32 v56, v56, v69
	v_mul_f32_e32 v57, v57, v58
	v_mul_f32_e32 v50, v52, v70
	v_mul_f32_e32 v51, v53, v59
	v_cvt_pk_fp8_f32 v62, v56, v57 op_sel:[0,0,1]
	v_cvt_pk_fp8_f32 v63, v50, v51 op_sel:[0,0,1]
	v_ashrrev_i32_e32 v65, 31, v64
	v_lshl_add_u64 v[50:51], v[64:65], 3, s[14:15]
	v_lshl_add_u64 v[50:51], v[50:51], 0, s[6:7]
	global_store_dwordx2 v[60:61], v[62:63], off offset:128
	v_mov_b32_e32 v52, 0
	v_mov_b32_e32 v53, 0
	v_add_u32_e32 v54, 0x90, v134
	v_ashrrev_i32_e32 v55, 31, v54
	v_add_u32_e32 v56, 0x2c0, v130
	v_lshlrev_b64 v[54:55], 11, v[54:55]
	v_ashrrev_i32_e32 v57, 31, v56
	v_lshl_add_u64 v[54:55], s[18:19], 0, v[54:55]
	s_waitcnt vmcnt(15)
	v_cvt_f32_ubyte0_e32 v58, v178
	v_cvt_f32_ubyte0_e32 v59, v179
	v_cvt_f32_ubyte1_e32 v60, v178
	v_cvt_f32_ubyte1_e32 v61, v179
	v_mul_f32_e32 v58, v141, v58
	v_mul_f32_e32 v59, v141, v59
	v_mul_f32_e32 v60, v141, v60
	v_mul_f32_e32 v61, v141, v61
	v_mul_f32_e32 v46, v46, v58
	v_mul_f32_e32 v47, v47, v60
	v_mul_f32_e32 v42, v42, v59
	v_mul_f32_e32 v43, v43, v61
	v_cvt_pk_fp8_f32 v52, v46, v47
	v_cvt_pk_fp8_f32 v53, v42, v43
	v_cvt_f32_ubyte2_e32 v62, v178
	v_cvt_f32_ubyte2_e32 v63, v179
	v_cvt_f32_ubyte3_e32 v50, v178
	v_cvt_f32_ubyte3_e32 v51, v179
	v_mul_f32_e32 v62, v141, v62
	v_mul_f32_e32 v63, v141, v63
	v_mul_f32_e32 v50, v141, v50
	v_mul_f32_e32 v51, v141, v51
	v_mul_f32_e32 v48, v48, v62
	v_mul_f32_e32 v49, v49, v50
	v_mul_f32_e32 v42, v44, v63
	v_mul_f32_e32 v43, v45, v51
	v_cvt_pk_fp8_f32 v52, v48, v49 op_sel:[0,0,1]
	v_cvt_pk_fp8_f32 v53, v42, v43 op_sel:[0,0,1]
	v_lshl_add_u64 v[42:43], v[56:57], 3, s[14:15]
	v_lshl_add_u64 v[44:45], v[54:55], 0, v[132:133]
	v_lshl_add_u64 v[42:43], v[42:43], 0, s[6:7]
	global_store_dwordx2 v[44:45], v[52:53], off
	v_mov_b32_e32 v46, 0
	v_mov_b32_e32 v47, 0
	v_add_u32_e32 v48, 0x300, v130
	s_waitcnt vmcnt(15)
	v_cvt_f32_ubyte0_e32 v49, v180
	v_cvt_f32_ubyte0_e32 v50, v181
	v_cvt_f32_ubyte1_e32 v51, v180
	v_cvt_f32_ubyte1_e32 v52, v181
	v_mul_f32_e32 v49, v141, v49
	v_mul_f32_e32 v50, v141, v50
	v_mul_f32_e32 v51, v141, v51
	v_mul_f32_e32 v52, v141, v52
	v_mul_f32_e32 v38, v38, v49
	v_mul_f32_e32 v39, v39, v51
	v_mul_f32_e32 v34, v34, v50
	v_mul_f32_e32 v35, v35, v52
	v_cvt_pk_fp8_f32 v46, v38, v39
	v_cvt_pk_fp8_f32 v47, v34, v35
	v_cvt_f32_ubyte2_e32 v53, v180
	v_cvt_f32_ubyte2_e32 v54, v181
	v_cvt_f32_ubyte3_e32 v42, v180
	v_cvt_f32_ubyte3_e32 v43, v181
	v_mul_f32_e32 v53, v141, v53
	v_mul_f32_e32 v54, v141, v54
	v_mul_f32_e32 v42, v141, v42
	v_mul_f32_e32 v43, v141, v43
	v_mul_f32_e32 v40, v40, v53
	v_mul_f32_e32 v41, v41, v42
	v_mul_f32_e32 v34, v36, v54
	v_mul_f32_e32 v35, v37, v43
	v_cvt_pk_fp8_f32 v46, v40, v41 op_sel:[0,0,1]
	v_cvt_pk_fp8_f32 v47, v34, v35 op_sel:[0,0,1]
	v_ashrrev_i32_e32 v49, 31, v48
	v_lshl_add_u64 v[34:35], v[48:49], 3, s[14:15]
	v_lshl_add_u64 v[34:35], v[34:35], 0, s[6:7]
	global_store_dwordx2 v[44:45], v[46:47], off offset:128
	v_mov_b32_e32 v36, 0
	v_mov_b32_e32 v37, 0
	v_add_u32_e32 v38, 0xa0, v134
	v_ashrrev_i32_e32 v39, 31, v38
	v_add_u32_e32 v40, 0x340, v130
	v_lshlrev_b64 v[38:39], 11, v[38:39]
	v_ashrrev_i32_e32 v41, 31, v40
	v_lshl_add_u64 v[38:39], s[18:19], 0, v[38:39]
	s_waitcnt vmcnt(15)
	v_cvt_f32_ubyte0_e32 v42, v182
	v_cvt_f32_ubyte0_e32 v43, v183
	v_cvt_f32_ubyte1_e32 v44, v182
	v_cvt_f32_ubyte1_e32 v45, v183
	v_mul_f32_e32 v42, v141, v42
	v_mul_f32_e32 v43, v141, v43
	v_mul_f32_e32 v44, v141, v44
	v_mul_f32_e32 v45, v141, v45
	v_mul_f32_e32 v30, v30, v42
	v_mul_f32_e32 v31, v31, v44
	v_mul_f32_e32 v26, v26, v43
	v_mul_f32_e32 v27, v27, v45
	v_cvt_pk_fp8_f32 v36, v30, v31
	v_cvt_pk_fp8_f32 v37, v26, v27
	v_cvt_f32_ubyte2_e32 v46, v182
	v_cvt_f32_ubyte2_e32 v47, v183
	v_cvt_f32_ubyte3_e32 v34, v182
	v_cvt_f32_ubyte3_e32 v35, v183
	v_mul_f32_e32 v46, v141, v46
	v_mul_f32_e32 v47, v141, v47
	v_mul_f32_e32 v34, v141, v34
	v_mul_f32_e32 v35, v141, v35
	v_mul_f32_e32 v32, v32, v46
	v_mul_f32_e32 v33, v33, v34
	v_mul_f32_e32 v26, v28, v47
	v_mul_f32_e32 v27, v29, v35
	v_cvt_pk_fp8_f32 v36, v32, v33 op_sel:[0,0,1]
	v_cvt_pk_fp8_f32 v37, v26, v27 op_sel:[0,0,1]
	v_lshl_add_u64 v[26:27], v[40:41], 3, s[14:15]
	v_lshl_add_u64 v[28:29], v[38:39], 0, v[132:133]
	v_lshl_add_u64 v[26:27], v[26:27], 0, s[6:7]
	global_store_dwordx2 v[28:29], v[36:37], off
	v_mov_b32_e32 v30, 0
	v_mov_b32_e32 v31, 0
	v_add_u32_e32 v32, 0x380, v130
	s_waitcnt vmcnt(15)
	v_cvt_f32_ubyte0_e32 v33, v184
	v_cvt_f32_ubyte0_e32 v34, v185
	v_cvt_f32_ubyte1_e32 v35, v184
	v_cvt_f32_ubyte1_e32 v36, v185
	v_mul_f32_e32 v33, v141, v33
	v_mul_f32_e32 v34, v141, v34
	v_mul_f32_e32 v35, v141, v35
	v_mul_f32_e32 v36, v141, v36
	v_mul_f32_e32 v22, v22, v33
	v_mul_f32_e32 v23, v23, v35
	v_mul_f32_e32 v18, v18, v34
	v_mul_f32_e32 v19, v19, v36
	v_cvt_pk_fp8_f32 v30, v22, v23
	v_cvt_pk_fp8_f32 v31, v18, v19
	v_cvt_f32_ubyte2_e32 v37, v184
	v_cvt_f32_ubyte2_e32 v38, v185
	v_cvt_f32_ubyte3_e32 v26, v184
	v_cvt_f32_ubyte3_e32 v27, v185
	v_mul_f32_e32 v37, v141, v37
	v_mul_f32_e32 v38, v141, v38
	v_mul_f32_e32 v26, v141, v26
	v_mul_f32_e32 v27, v141, v27
	v_mul_f32_e32 v24, v24, v37
	v_mul_f32_e32 v25, v25, v26
	v_mul_f32_e32 v18, v20, v38
	v_mul_f32_e32 v19, v21, v27
	v_cvt_pk_fp8_f32 v30, v24, v25 op_sel:[0,0,1]
	v_cvt_pk_fp8_f32 v31, v18, v19 op_sel:[0,0,1]
	v_ashrrev_i32_e32 v33, 31, v32
	v_lshl_add_u64 v[18:19], v[32:33], 3, s[14:15]
	v_lshl_add_u64 v[18:19], v[18:19], 0, s[6:7]
	global_store_dwordx2 v[28:29], v[30:31], off offset:128
	v_mov_b32_e32 v20, 0
	v_mov_b32_e32 v21, 0
	v_add_u32_e32 v22, 0xb0, v134
	v_ashrrev_i32_e32 v23, 31, v22
	v_add_u32_e32 v24, 0x3c0, v130
	v_lshlrev_b64 v[22:23], 11, v[22:23]
	v_ashrrev_i32_e32 v25, 31, v24
	v_lshl_add_u64 v[22:23], s[18:19], 0, v[22:23]
	s_waitcnt vmcnt(15)
	v_cvt_f32_ubyte0_e32 v26, v186
	v_cvt_f32_ubyte0_e32 v27, v187
	v_cvt_f32_ubyte1_e32 v28, v186
	v_cvt_f32_ubyte1_e32 v29, v187
	v_mul_f32_e32 v26, v141, v26
	v_mul_f32_e32 v27, v141, v27
	v_mul_f32_e32 v28, v141, v28
	v_mul_f32_e32 v29, v141, v29
	v_mul_f32_e32 v14, v14, v26
	v_mul_f32_e32 v15, v15, v28
	v_mul_f32_e32 v10, v10, v27
	v_mul_f32_e32 v11, v11, v29
	v_cvt_pk_fp8_f32 v20, v14, v15
	v_cvt_pk_fp8_f32 v21, v10, v11
	v_cvt_f32_ubyte2_e32 v30, v186
	v_cvt_f32_ubyte2_e32 v31, v187
	v_cvt_f32_ubyte3_e32 v18, v186
	v_cvt_f32_ubyte3_e32 v19, v187
	v_mul_f32_e32 v30, v141, v30
	v_mul_f32_e32 v31, v141, v31
	v_mul_f32_e32 v18, v141, v18
	v_mul_f32_e32 v19, v141, v19
	v_mul_f32_e32 v16, v16, v30
	v_mul_f32_e32 v17, v17, v18
	v_mul_f32_e32 v10, v12, v31
	v_mul_f32_e32 v11, v13, v19
	v_cvt_pk_fp8_f32 v20, v16, v17 op_sel:[0,0,1]
	v_cvt_pk_fp8_f32 v21, v10, v11 op_sel:[0,0,1]
	v_lshl_add_u64 v[10:11], v[24:25], 3, s[14:15]
	v_lshl_add_u64 v[12:13], v[22:23], 0, v[132:133]
	v_lshl_add_u64 v[10:11], v[10:11], 0, s[6:7]
	global_store_dwordx2 v[12:13], v[20:21], off
	v_mov_b32_e32 v14, 0
	v_mov_b32_e32 v15, 0
	s_mov_b64 s[6:7], -1
	s_waitcnt vmcnt(15)
	v_cvt_f32_ubyte0_e32 v16, v188
	v_cvt_f32_ubyte0_e32 v17, v189
	v_cvt_f32_ubyte1_e32 v18, v188
	v_cvt_f32_ubyte1_e32 v19, v189
	v_mul_f32_e32 v16, v141, v16
	v_mul_f32_e32 v17, v141, v17
	v_mul_f32_e32 v18, v141, v18
	v_mul_f32_e32 v19, v141, v19
	v_mul_f32_e32 v6, v6, v16
	v_mul_f32_e32 v7, v7, v18
	v_mul_f32_e32 v2, v2, v17
	v_mul_f32_e32 v3, v3, v19
	v_cvt_pk_fp8_f32 v14, v6, v7
	v_cvt_pk_fp8_f32 v15, v2, v3
	v_cvt_f32_ubyte2_e32 v20, v188
	v_cvt_f32_ubyte2_e32 v21, v189
	v_cvt_f32_ubyte3_e32 v10, v188
	v_cvt_f32_ubyte3_e32 v11, v189
	v_mul_f32_e32 v20, v141, v20
	v_mul_f32_e32 v21, v141, v21
	v_mul_f32_e32 v10, v141, v10
	v_mul_f32_e32 v11, v141, v11
	v_mul_f32_e32 v8, v8, v20
	v_mul_f32_e32 v9, v9, v10
	v_mul_f32_e32 v2, v4, v21
	v_mul_f32_e32 v3, v5, v11
	v_cvt_pk_fp8_f32 v14, v8, v9 op_sel:[0,0,1]
	v_cvt_pk_fp8_f32 v15, v2, v3 op_sel:[0,0,1]
	global_store_dwordx2 v[12:13], v[14:15], off offset:128
	s_cbranch_vccnz .LBB0_1514
	s_andn2_b64 vcc, exec, s[16:17]
	s_cbranch_vccnz .LBB0_1513
	s_barrier
	s_branch .LBB0_1513

.LBB0_3043:
	v_mov_b32_e32 v134, v143
	v_mov_b32_e32 v135, v142
	s_lshl_b32 s6, s63, 3
	s_add_i32 s6, s6, s64
	v_lshlrev_b32_e32 v130, 4, v135
	s_addk_i32 s6, 0x630
	v_add3_u32 v130, v134, s57, v130
	s_ashr_i32 s7, s6, 31
	v_ashrrev_i32_e32 v131, 31, v130
	s_lshl_b64 s[6:7], s[6:7], 16
	v_lshl_add_u64 v[132:133], v[130:131], 3, s[16:17]
	v_lshl_add_u64 v[132:133], v[132:133], 0, s[6:7]
	global_load_dwordx2 v[136:137], v[132:133], off
	s_mov_b64 s[98:99], 0x1000
	v_lshl_add_u64 v[190:191], v[132:133], 0, s[98:99]
	global_load_dwordx2 v[160:161], v[132:133], off offset:512
	global_load_dwordx2 v[162:163], v[132:133], off offset:1024
	global_load_dwordx2 v[164:165], v[132:133], off offset:1536
	global_load_dwordx2 v[166:167], v[132:133], off offset:2048
	global_load_dwordx2 v[168:169], v[132:133], off offset:2560
	global_load_dwordx2 v[170:171], v[132:133], off offset:3072
	global_load_dwordx2 v[172:173], v[132:133], off offset:3584
	global_load_dwordx2 v[174:175], v[190:191], off
	global_load_dwordx2 v[176:177], v[190:191], off offset:512
	global_load_dwordx2 v[178:179], v[190:191], off offset:1024
	global_load_dwordx2 v[180:181], v[190:191], off offset:1536
	global_load_dwordx2 v[182:183], v[190:191], off offset:2048
	global_load_dwordx2 v[184:185], v[190:191], off offset:2560
	global_load_dwordx2 v[186:187], v[190:191], off offset:3072
	global_load_dwordx2 v[188:189], v[190:191], off offset:3584
	s_lshl_b32 s26, s63, 8
	s_lshl_b32 s27, s64, 8
	s_add_i32 s26, s26, s54
	s_or_b32 s27, s27, s55
	v_add_u32_e32 v134, s26, v134
	v_lshl_add_u32 v132, v135, 3, s27
	v_ashrrev_i32_e32 v135, 31, v134
	v_lshlrev_b64 v[152:153], 11, v[134:135]
	v_mov_b32_e32 v150, 0
	v_mov_b32_e32 v151, 0
	v_add_u32_e32 v154, 64, v130
	v_ashrrev_i32_e32 v133, 31, v132
	v_lshl_add_u64 v[152:153], s[18:19], 0, v[152:153]
	v_ashrrev_i32_e32 v155, 31, v154
	s_andn2_b64 vcc, exec, s[24:25]
	s_waitcnt vmcnt(15)
	v_cvt_f32_ubyte0_e32 v131, v136
	v_cvt_f32_ubyte0_e32 v135, v137
	v_cvt_f32_ubyte1_e32 v149, v136
	v_cvt_f32_ubyte1_e32 v156, v137
	v_mul_f32_e32 v131, v141, v131
	v_mul_f32_e32 v135, v141, v135
	v_mul_f32_e32 v149, v141, v149
	v_mul_f32_e32 v156, v141, v156
	v_mul_f32_e32 v126, v126, v131
	v_mul_f32_e32 v127, v127, v149
	v_mul_f32_e32 v122, v122, v135
	v_mul_f32_e32 v123, v123, v156
	v_cvt_pk_fp8_f32 v150, v126, v127
	v_cvt_pk_fp8_f32 v151, v122, v123
	v_cvt_f32_ubyte2_e32 v157, v136
	v_cvt_f32_ubyte2_e32 v158, v137
	v_cvt_f32_ubyte3_e32 v136, v136
	v_cvt_f32_ubyte3_e32 v137, v137
	v_mul_f32_e32 v157, v141, v157
	v_mul_f32_e32 v158, v141, v158
	v_mul_f32_e32 v136, v141, v136
	v_mul_f32_e32 v137, v141, v137
	v_mul_f32_e32 v128, v128, v157
	v_mul_f32_e32 v129, v129, v136
	v_mul_f32_e32 v122, v124, v158
	v_mul_f32_e32 v123, v125, v137
	v_cvt_pk_fp8_f32 v150, v128, v129 op_sel:[0,0,1]
	v_cvt_pk_fp8_f32 v151, v122, v123 op_sel:[0,0,1]
	v_lshl_add_u64 v[122:123], v[152:153], 0, v[132:133]
	v_lshl_add_u64 v[124:125], v[154:155], 3, s[16:17]
	v_lshl_add_u64 v[124:125], v[124:125], 0, s[6:7]
	global_store_dwordx2 v[122:123], v[150:151], off
	v_mov_b32_e32 v126, 0
	v_mov_b32_e32 v127, 0
	v_add_u32_e32 v128, 0x80, v130
	s_waitcnt vmcnt(15)
	v_cvt_f32_ubyte0_e32 v129, v160
	v_cvt_f32_ubyte0_e32 v131, v161
	v_cvt_f32_ubyte1_e32 v135, v160
	v_cvt_f32_ubyte1_e32 v136, v161
	v_mul_f32_e32 v129, v141, v129
	v_mul_f32_e32 v131, v141, v131
	v_mul_f32_e32 v135, v141, v135
	v_mul_f32_e32 v136, v141, v136
	v_mul_f32_e32 v118, v118, v129
	v_mul_f32_e32 v119, v119, v135
	v_mul_f32_e32 v114, v114, v131
	v_mul_f32_e32 v115, v115, v136
	v_cvt_pk_fp8_f32 v126, v118, v119
	v_cvt_pk_fp8_f32 v127, v114, v115
	v_cvt_f32_ubyte2_e32 v137, v160
	v_cvt_f32_ubyte2_e32 v149, v161
	v_cvt_f32_ubyte3_e32 v124, v160
	v_cvt_f32_ubyte3_e32 v125, v161
	v_mul_f32_e32 v137, v141, v137
	v_mul_f32_e32 v149, v141, v149
	v_mul_f32_e32 v124, v141, v124
	v_mul_f32_e32 v125, v141, v125
	v_mul_f32_e32 v120, v120, v137
	v_mul_f32_e32 v121, v121, v124
	v_mul_f32_e32 v114, v116, v149
	v_mul_f32_e32 v115, v117, v125
	v_cvt_pk_fp8_f32 v126, v120, v121 op_sel:[0,0,1]
	v_cvt_pk_fp8_f32 v127, v114, v115 op_sel:[0,0,1]
	v_ashrrev_i32_e32 v129, 31, v128
	v_lshl_add_u64 v[114:115], v[128:129], 3, s[16:17]
	v_lshl_add_u64 v[114:115], v[114:115], 0, s[6:7]
	global_store_dwordx2 v[122:123], v[126:127], off offset:128
	v_mov_b32_e32 v116, 0
	v_mov_b32_e32 v117, 0
	v_add_u32_e32 v118, 16, v134
	v_ashrrev_i32_e32 v119, 31, v118
	v_add_u32_e32 v120, 0xc0, v130
	v_lshlrev_b64 v[118:119], 11, v[118:119]
	v_ashrrev_i32_e32 v121, 31, v120
	v_lshl_add_u64 v[118:119], s[18:19], 0, v[118:119]
	s_waitcnt vmcnt(15)
	v_cvt_f32_ubyte0_e32 v122, v162
	v_cvt_f32_ubyte0_e32 v123, v163
	v_cvt_f32_ubyte1_e32 v124, v162
	v_cvt_f32_ubyte1_e32 v125, v163
	v_mul_f32_e32 v122, v141, v122
	v_mul_f32_e32 v123, v141, v123
	v_mul_f32_e32 v124, v141, v124
	v_mul_f32_e32 v125, v141, v125
	v_mul_f32_e32 v110, v110, v122
	v_mul_f32_e32 v111, v111, v124
	v_mul_f32_e32 v106, v106, v123
	v_mul_f32_e32 v107, v107, v125
	v_cvt_pk_fp8_f32 v116, v110, v111
	v_cvt_pk_fp8_f32 v117, v106, v107
	v_cvt_f32_ubyte2_e32 v126, v162
	v_cvt_f32_ubyte2_e32 v127, v163
	v_cvt_f32_ubyte3_e32 v114, v162
	v_cvt_f32_ubyte3_e32 v115, v163
	v_mul_f32_e32 v126, v141, v126
	v_mul_f32_e32 v127, v141, v127
	v_mul_f32_e32 v114, v141, v114
	v_mul_f32_e32 v115, v141, v115
	v_mul_f32_e32 v112, v112, v126
	v_mul_f32_e32 v113, v113, v114
	v_mul_f32_e32 v106, v108, v127
	v_mul_f32_e32 v107, v109, v115
	v_cvt_pk_fp8_f32 v116, v112, v113 op_sel:[0,0,1]
	v_cvt_pk_fp8_f32 v117, v106, v107 op_sel:[0,0,1]
	v_lshl_add_u64 v[106:107], v[120:121], 3, s[16:17]
	v_lshl_add_u64 v[108:109], v[118:119], 0, v[132:133]
	v_lshl_add_u64 v[106:107], v[106:107], 0, s[6:7]
	global_store_dwordx2 v[108:109], v[116:117], off
	v_mov_b32_e32 v110, 0
	v_mov_b32_e32 v111, 0
	v_add_u32_e32 v112, 0x100, v130
	s_waitcnt vmcnt(15)
	v_cvt_f32_ubyte0_e32 v113, v164
	v_cvt_f32_ubyte0_e32 v114, v165
	v_cvt_f32_ubyte1_e32 v115, v164
	v_cvt_f32_ubyte1_e32 v116, v165
	v_mul_f32_e32 v113, v141, v113
	v_mul_f32_e32 v114, v141, v114
	v_mul_f32_e32 v115, v141, v115
	v_mul_f32_e32 v116, v141, v116
	v_mul_f32_e32 v102, v102, v113
	v_mul_f32_e32 v103, v103, v115
	v_mul_f32_e32 v98, v98, v114
	v_mul_f32_e32 v99, v99, v116
	v_cvt_pk_fp8_f32 v110, v102, v103
	v_cvt_pk_fp8_f32 v111, v98, v99
	v_cvt_f32_ubyte2_e32 v117, v164
	v_cvt_f32_ubyte2_e32 v118, v165
	v_cvt_f32_ubyte3_e32 v106, v164
	v_cvt_f32_ubyte3_e32 v107, v165
	v_mul_f32_e32 v117, v141, v117
	v_mul_f32_e32 v118, v141, v118
	v_mul_f32_e32 v106, v141, v106
	v_mul_f32_e32 v107, v141, v107
	v_mul_f32_e32 v104, v104, v117
	v_mul_f32_e32 v105, v105, v106
	v_mul_f32_e32 v98, v100, v118
	v_mul_f32_e32 v99, v101, v107
	v_cvt_pk_fp8_f32 v110, v104, v105 op_sel:[0,0,1]
	v_cvt_pk_fp8_f32 v111, v98, v99 op_sel:[0,0,1]
	v_ashrrev_i32_e32 v113, 31, v112
	v_lshl_add_u64 v[98:99], v[112:113], 3, s[16:17]
	v_lshl_add_u64 v[98:99], v[98:99], 0, s[6:7]
	global_store_dwordx2 v[108:109], v[110:111], off offset:128
	v_mov_b32_e32 v100, 0
	v_mov_b32_e32 v101, 0
	v_add_u32_e32 v102, 32, v134
	v_ashrrev_i32_e32 v103, 31, v102
	v_add_u32_e32 v104, 0x140, v130
	v_lshlrev_b64 v[102:103], 11, v[102:103]
	v_ashrrev_i32_e32 v105, 31, v104
	v_lshl_add_u64 v[102:103], s[18:19], 0, v[102:103]
	s_waitcnt vmcnt(15)
	v_cvt_f32_ubyte0_e32 v106, v166
	v_cvt_f32_ubyte0_e32 v107, v167
	v_cvt_f32_ubyte1_e32 v108, v166
	v_cvt_f32_ubyte1_e32 v109, v167
	v_mul_f32_e32 v106, v141, v106
	v_mul_f32_e32 v107, v141, v107
	v_mul_f32_e32 v108, v141, v108
	v_mul_f32_e32 v109, v141, v109
	v_mul_f32_e32 v94, v94, v106
	v_mul_f32_e32 v95, v95, v108
	v_mul_f32_e32 v90, v90, v107
	v_mul_f32_e32 v91, v91, v109
	v_cvt_pk_fp8_f32 v100, v94, v95
	v_cvt_pk_fp8_f32 v101, v90, v91
	v_cvt_f32_ubyte2_e32 v110, v166
	v_cvt_f32_ubyte2_e32 v111, v167
	v_cvt_f32_ubyte3_e32 v98, v166
	v_cvt_f32_ubyte3_e32 v99, v167
	v_mul_f32_e32 v110, v141, v110
	v_mul_f32_e32 v111, v141, v111
	v_mul_f32_e32 v98, v141, v98
	v_mul_f32_e32 v99, v141, v99
	v_mul_f32_e32 v96, v96, v110
	v_mul_f32_e32 v97, v97, v98
	v_mul_f32_e32 v90, v92, v111
	v_mul_f32_e32 v91, v93, v99
	v_cvt_pk_fp8_f32 v100, v96, v97 op_sel:[0,0,1]
	v_cvt_pk_fp8_f32 v101, v90, v91 op_sel:[0,0,1]
	v_lshl_add_u64 v[90:91], v[104:105], 3, s[16:17]
	v_lshl_add_u64 v[92:93], v[102:103], 0, v[132:133]
	v_lshl_add_u64 v[90:91], v[90:91], 0, s[6:7]
	global_store_dwordx2 v[92:93], v[100:101], off
	v_mov_b32_e32 v94, 0
	v_mov_b32_e32 v95, 0
	v_add_u32_e32 v96, 0x180, v130
	s_waitcnt vmcnt(15)
	v_cvt_f32_ubyte0_e32 v97, v168
	v_cvt_f32_ubyte0_e32 v98, v169
	v_cvt_f32_ubyte1_e32 v99, v168
	v_cvt_f32_ubyte1_e32 v100, v169
	v_mul_f32_e32 v97, v141, v97
	v_mul_f32_e32 v98, v141, v98
	v_mul_f32_e32 v99, v141, v99
	v_mul_f32_e32 v100, v141, v100
	v_mul_f32_e32 v86, v86, v97
	v_mul_f32_e32 v87, v87, v99
	v_mul_f32_e32 v82, v82, v98
	v_mul_f32_e32 v83, v83, v100
	v_cvt_pk_fp8_f32 v94, v86, v87
	v_cvt_pk_fp8_f32 v95, v82, v83
	v_cvt_f32_ubyte2_e32 v101, v168
	v_cvt_f32_ubyte2_e32 v102, v169
	v_cvt_f32_ubyte3_e32 v90, v168
	v_cvt_f32_ubyte3_e32 v91, v169
	v_mul_f32_e32 v101, v141, v101
	v_mul_f32_e32 v102, v141, v102
	v_mul_f32_e32 v90, v141, v90
	v_mul_f32_e32 v91, v141, v91
	v_mul_f32_e32 v88, v88, v101
	v_mul_f32_e32 v89, v89, v90
	v_mul_f32_e32 v82, v84, v102
	v_mul_f32_e32 v83, v85, v91
	v_cvt_pk_fp8_f32 v94, v88, v89 op_sel:[0,0,1]
	v_cvt_pk_fp8_f32 v95, v82, v83 op_sel:[0,0,1]
	v_ashrrev_i32_e32 v97, 31, v96
	v_lshl_add_u64 v[82:83], v[96:97], 3, s[16:17]
	v_lshl_add_u64 v[82:83], v[82:83], 0, s[6:7]
	global_store_dwordx2 v[92:93], v[94:95], off offset:128
	v_mov_b32_e32 v84, 0
	v_mov_b32_e32 v85, 0
	v_add_u32_e32 v86, 48, v134
	v_ashrrev_i32_e32 v87, 31, v86
	v_add_u32_e32 v88, 0x1c0, v130
	v_lshlrev_b64 v[86:87], 11, v[86:87]
	v_ashrrev_i32_e32 v89, 31, v88
	v_lshl_add_u64 v[86:87], s[18:19], 0, v[86:87]
	s_waitcnt vmcnt(15)
	v_cvt_f32_ubyte0_e32 v90, v170
	v_cvt_f32_ubyte0_e32 v91, v171
	v_cvt_f32_ubyte1_e32 v92, v170
	v_cvt_f32_ubyte1_e32 v93, v171
	v_mul_f32_e32 v90, v141, v90
	v_mul_f32_e32 v91, v141, v91
	v_mul_f32_e32 v92, v141, v92
	v_mul_f32_e32 v93, v141, v93
	v_mul_f32_e32 v78, v78, v90
	v_mul_f32_e32 v79, v79, v92
	v_mul_f32_e32 v74, v74, v91
	v_mul_f32_e32 v75, v75, v93
	v_cvt_pk_fp8_f32 v84, v78, v79
	v_cvt_pk_fp8_f32 v85, v74, v75
	v_cvt_f32_ubyte2_e32 v94, v170
	v_cvt_f32_ubyte2_e32 v95, v171
	v_cvt_f32_ubyte3_e32 v82, v170
	v_cvt_f32_ubyte3_e32 v83, v171
	v_mul_f32_e32 v94, v141, v94
	v_mul_f32_e32 v95, v141, v95
	v_mul_f32_e32 v82, v141, v82
	v_mul_f32_e32 v83, v141, v83
	v_mul_f32_e32 v80, v80, v94
	v_mul_f32_e32 v81, v81, v82
	v_mul_f32_e32 v74, v76, v95
	v_mul_f32_e32 v75, v77, v83
	v_cvt_pk_fp8_f32 v84, v80, v81 op_sel:[0,0,1]
	v_cvt_pk_fp8_f32 v85, v74, v75 op_sel:[0,0,1]
	v_lshl_add_u64 v[74:75], v[88:89], 3, s[16:17]
	v_lshl_add_u64 v[76:77], v[86:87], 0, v[132:133]
	v_lshl_add_u64 v[74:75], v[74:75], 0, s[6:7]
	global_store_dwordx2 v[76:77], v[84:85], off
	v_mov_b32_e32 v78, 0
	v_mov_b32_e32 v79, 0
	v_add_u32_e32 v80, 0x200, v130
	s_waitcnt vmcnt(15)
	v_cvt_f32_ubyte0_e32 v81, v172
	v_cvt_f32_ubyte0_e32 v82, v173
	v_cvt_f32_ubyte1_e32 v83, v172
	v_cvt_f32_ubyte1_e32 v84, v173
	v_mul_f32_e32 v81, v141, v81
	v_mul_f32_e32 v82, v141, v82
	v_mul_f32_e32 v83, v141, v83
	v_mul_f32_e32 v84, v141, v84
	v_mul_f32_e32 v70, v70, v81
	v_mul_f32_e32 v71, v71, v83
	v_mul_f32_e32 v66, v66, v82
	v_mul_f32_e32 v67, v67, v84
	v_cvt_pk_fp8_f32 v78, v70, v71
	v_cvt_pk_fp8_f32 v79, v66, v67
	v_cvt_f32_ubyte2_e32 v85, v172
	v_cvt_f32_ubyte2_e32 v86, v173
	v_cvt_f32_ubyte3_e32 v74, v172
	v_cvt_f32_ubyte3_e32 v75, v173
	v_mul_f32_e32 v85, v141, v85
	v_mul_f32_e32 v86, v141, v86
	v_mul_f32_e32 v74, v141, v74
	v_mul_f32_e32 v75, v141, v75
	v_mul_f32_e32 v72, v72, v85
	v_mul_f32_e32 v73, v73, v74
	v_mul_f32_e32 v66, v68, v86
	v_mul_f32_e32 v67, v69, v75
	v_cvt_pk_fp8_f32 v78, v72, v73 op_sel:[0,0,1]
	v_cvt_pk_fp8_f32 v79, v66, v67 op_sel:[0,0,1]
	v_ashrrev_i32_e32 v81, 31, v80
	v_lshl_add_u64 v[66:67], v[80:81], 3, s[16:17]
	v_lshl_add_u64 v[66:67], v[66:67], 0, s[6:7]
	global_store_dwordx2 v[76:77], v[78:79], off offset:128
	v_mov_b32_e32 v68, 0
	v_mov_b32_e32 v69, 0
	v_add_u32_e32 v70, 0x80, v134
	v_ashrrev_i32_e32 v71, 31, v70
	v_add_u32_e32 v72, 0x240, v130
	v_lshlrev_b64 v[70:71], 11, v[70:71]
	v_ashrrev_i32_e32 v73, 31, v72
	v_lshl_add_u64 v[70:71], s[18:19], 0, v[70:71]
	s_waitcnt vmcnt(15)
	v_cvt_f32_ubyte0_e32 v74, v174
	v_cvt_f32_ubyte0_e32 v75, v175
	v_cvt_f32_ubyte1_e32 v76, v174
	v_cvt_f32_ubyte1_e32 v77, v175
	v_mul_f32_e32 v74, v141, v74
	v_mul_f32_e32 v75, v141, v75
	v_mul_f32_e32 v76, v141, v76
	v_mul_f32_e32 v77, v141, v77
	v_mul_f32_e32 v62, v62, v74
	v_mul_f32_e32 v63, v63, v76
	v_mul_f32_e32 v58, v58, v75
	v_mul_f32_e32 v59, v59, v77
	v_cvt_pk_fp8_f32 v68, v62, v63
	v_cvt_pk_fp8_f32 v69, v58, v59
	v_cvt_f32_ubyte2_e32 v78, v174
	v_cvt_f32_ubyte2_e32 v79, v175
	v_cvt_f32_ubyte3_e32 v66, v174
	v_cvt_f32_ubyte3_e32 v67, v175
	v_mul_f32_e32 v78, v141, v78
	v_mul_f32_e32 v79, v141, v79
	v_mul_f32_e32 v66, v141, v66
	v_mul_f32_e32 v67, v141, v67
	v_mul_f32_e32 v64, v64, v78
	v_mul_f32_e32 v65, v65, v66
	v_mul_f32_e32 v58, v60, v79
	v_mul_f32_e32 v59, v61, v67
	v_cvt_pk_fp8_f32 v68, v64, v65 op_sel:[0,0,1]
	v_cvt_pk_fp8_f32 v69, v58, v59 op_sel:[0,0,1]
	v_lshl_add_u64 v[58:59], v[72:73], 3, s[16:17]
	v_lshl_add_u64 v[60:61], v[70:71], 0, v[132:133]
	v_lshl_add_u64 v[58:59], v[58:59], 0, s[6:7]
	global_store_dwordx2 v[60:61], v[68:69], off
	v_mov_b32_e32 v62, 0
	v_mov_b32_e32 v63, 0
	v_add_u32_e32 v64, 0x280, v130
	s_waitcnt vmcnt(15)
	v_cvt_f32_ubyte0_e32 v65, v176
	v_cvt_f32_ubyte0_e32 v66, v177
	v_cvt_f32_ubyte1_e32 v67, v176
	v_cvt_f32_ubyte1_e32 v68, v177
	v_mul_f32_e32 v65, v141, v65
	v_mul_f32_e32 v66, v141, v66
	v_mul_f32_e32 v67, v141, v67
	v_mul_f32_e32 v68, v141, v68
	v_mul_f32_e32 v54, v54, v65
	v_mul_f32_e32 v55, v55, v67
	v_mul_f32_e32 v50, v50, v66
	v_mul_f32_e32 v51, v51, v68
	v_cvt_pk_fp8_f32 v62, v54, v55
	v_cvt_pk_fp8_f32 v63, v50, v51
	v_cvt_f32_ubyte2_e32 v69, v176
	v_cvt_f32_ubyte2_e32 v70, v177
	v_cvt_f32_ubyte3_e32 v58, v176
	v_cvt_f32_ubyte3_e32 v59, v177
	v_mul_f32_e32 v69, v141, v69
	v_mul_f32_e32 v70, v141, v70
	v_mul_f32_e32 v58, v141, v58
	v_mul_f32_e32 v59, v141, v59
	v_mul_f32_e32 v56, v56, v69
	v_mul_f32_e32 v57, v57, v58
	v_mul_f32_e32 v50, v52, v70
	v_mul_f32_e32 v51, v53, v59
	v_cvt_pk_fp8_f32 v62, v56, v57 op_sel:[0,0,1]
	v_cvt_pk_fp8_f32 v63, v50, v51 op_sel:[0,0,1]
	v_ashrrev_i32_e32 v65, 31, v64
	v_lshl_add_u64 v[50:51], v[64:65], 3, s[16:17]
	v_lshl_add_u64 v[50:51], v[50:51], 0, s[6:7]
	global_store_dwordx2 v[60:61], v[62:63], off offset:128
	v_mov_b32_e32 v52, 0
	v_mov_b32_e32 v53, 0
	v_add_u32_e32 v54, 0x90, v134
	v_ashrrev_i32_e32 v55, 31, v54
	v_add_u32_e32 v56, 0x2c0, v130
	v_lshlrev_b64 v[54:55], 11, v[54:55]
	v_ashrrev_i32_e32 v57, 31, v56
	v_lshl_add_u64 v[54:55], s[18:19], 0, v[54:55]
	s_waitcnt vmcnt(15)
	v_cvt_f32_ubyte0_e32 v58, v178
	v_cvt_f32_ubyte0_e32 v59, v179
	v_cvt_f32_ubyte1_e32 v60, v178
	v_cvt_f32_ubyte1_e32 v61, v179
	v_mul_f32_e32 v58, v141, v58
	v_mul_f32_e32 v59, v141, v59
	v_mul_f32_e32 v60, v141, v60
	v_mul_f32_e32 v61, v141, v61
	v_mul_f32_e32 v46, v46, v58
	v_mul_f32_e32 v47, v47, v60
	v_mul_f32_e32 v42, v42, v59
	v_mul_f32_e32 v43, v43, v61
	v_cvt_pk_fp8_f32 v52, v46, v47
	v_cvt_pk_fp8_f32 v53, v42, v43
	v_cvt_f32_ubyte2_e32 v62, v178
	v_cvt_f32_ubyte2_e32 v63, v179
	v_cvt_f32_ubyte3_e32 v50, v178
	v_cvt_f32_ubyte3_e32 v51, v179
	v_mul_f32_e32 v62, v141, v62
	v_mul_f32_e32 v63, v141, v63
	v_mul_f32_e32 v50, v141, v50
	v_mul_f32_e32 v51, v141, v51
	v_mul_f32_e32 v48, v48, v62
	v_mul_f32_e32 v49, v49, v50
	v_mul_f32_e32 v42, v44, v63
	v_mul_f32_e32 v43, v45, v51
	v_cvt_pk_fp8_f32 v52, v48, v49 op_sel:[0,0,1]
	v_cvt_pk_fp8_f32 v53, v42, v43 op_sel:[0,0,1]
	v_lshl_add_u64 v[42:43], v[56:57], 3, s[16:17]
	v_lshl_add_u64 v[44:45], v[54:55], 0, v[132:133]
	v_lshl_add_u64 v[42:43], v[42:43], 0, s[6:7]
	global_store_dwordx2 v[44:45], v[52:53], off
	v_mov_b32_e32 v46, 0
	v_mov_b32_e32 v47, 0
	v_add_u32_e32 v48, 0x300, v130
	s_waitcnt vmcnt(15)
	v_cvt_f32_ubyte0_e32 v49, v180
	v_cvt_f32_ubyte0_e32 v50, v181
	v_cvt_f32_ubyte1_e32 v51, v180
	v_cvt_f32_ubyte1_e32 v52, v181
	v_mul_f32_e32 v49, v141, v49
	v_mul_f32_e32 v50, v141, v50
	v_mul_f32_e32 v51, v141, v51
	v_mul_f32_e32 v52, v141, v52
	v_mul_f32_e32 v38, v38, v49
	v_mul_f32_e32 v39, v39, v51
	v_mul_f32_e32 v34, v34, v50
	v_mul_f32_e32 v35, v35, v52
	v_cvt_pk_fp8_f32 v46, v38, v39
	v_cvt_pk_fp8_f32 v47, v34, v35
	v_cvt_f32_ubyte2_e32 v53, v180
	v_cvt_f32_ubyte2_e32 v54, v181
	v_cvt_f32_ubyte3_e32 v42, v180
	v_cvt_f32_ubyte3_e32 v43, v181
	v_mul_f32_e32 v53, v141, v53
	v_mul_f32_e32 v54, v141, v54
	v_mul_f32_e32 v42, v141, v42
	v_mul_f32_e32 v43, v141, v43
	v_mul_f32_e32 v40, v40, v53
	v_mul_f32_e32 v41, v41, v42
	v_mul_f32_e32 v34, v36, v54
	v_mul_f32_e32 v35, v37, v43
	v_cvt_pk_fp8_f32 v46, v40, v41 op_sel:[0,0,1]
	v_cvt_pk_fp8_f32 v47, v34, v35 op_sel:[0,0,1]
	v_ashrrev_i32_e32 v49, 31, v48
	v_lshl_add_u64 v[34:35], v[48:49], 3, s[16:17]
	v_lshl_add_u64 v[34:35], v[34:35], 0, s[6:7]
	global_store_dwordx2 v[44:45], v[46:47], off offset:128
	v_mov_b32_e32 v36, 0
	v_mov_b32_e32 v37, 0
	v_add_u32_e32 v38, 0xa0, v134
	v_ashrrev_i32_e32 v39, 31, v38
	v_add_u32_e32 v40, 0x340, v130
	v_lshlrev_b64 v[38:39], 11, v[38:39]
	v_ashrrev_i32_e32 v41, 31, v40
	v_lshl_add_u64 v[38:39], s[18:19], 0, v[38:39]
	s_waitcnt vmcnt(15)
	v_cvt_f32_ubyte0_e32 v42, v182
	v_cvt_f32_ubyte0_e32 v43, v183
	v_cvt_f32_ubyte1_e32 v44, v182
	v_cvt_f32_ubyte1_e32 v45, v183
	v_mul_f32_e32 v42, v141, v42
	v_mul_f32_e32 v43, v141, v43
	v_mul_f32_e32 v44, v141, v44
	v_mul_f32_e32 v45, v141, v45
	v_mul_f32_e32 v30, v30, v42
	v_mul_f32_e32 v31, v31, v44
	v_mul_f32_e32 v26, v26, v43
	v_mul_f32_e32 v27, v27, v45
	v_cvt_pk_fp8_f32 v36, v30, v31
	v_cvt_pk_fp8_f32 v37, v26, v27
	v_cvt_f32_ubyte2_e32 v46, v182
	v_cvt_f32_ubyte2_e32 v47, v183
	v_cvt_f32_ubyte3_e32 v34, v182
	v_cvt_f32_ubyte3_e32 v35, v183
	v_mul_f32_e32 v46, v141, v46
	v_mul_f32_e32 v47, v141, v47
	v_mul_f32_e32 v34, v141, v34
	v_mul_f32_e32 v35, v141, v35
	v_mul_f32_e32 v32, v32, v46
	v_mul_f32_e32 v33, v33, v34
	v_mul_f32_e32 v26, v28, v47
	v_mul_f32_e32 v27, v29, v35
	v_cvt_pk_fp8_f32 v36, v32, v33 op_sel:[0,0,1]
	v_cvt_pk_fp8_f32 v37, v26, v27 op_sel:[0,0,1]
	v_lshl_add_u64 v[26:27], v[40:41], 3, s[16:17]
	v_lshl_add_u64 v[28:29], v[38:39], 0, v[132:133]
	v_lshl_add_u64 v[26:27], v[26:27], 0, s[6:7]
	global_store_dwordx2 v[28:29], v[36:37], off
	v_mov_b32_e32 v30, 0
	v_mov_b32_e32 v31, 0
	v_add_u32_e32 v32, 0x380, v130
	s_waitcnt vmcnt(15)
	v_cvt_f32_ubyte0_e32 v33, v184
	v_cvt_f32_ubyte0_e32 v34, v185
	v_cvt_f32_ubyte1_e32 v35, v184
	v_cvt_f32_ubyte1_e32 v36, v185
	v_mul_f32_e32 v33, v141, v33
	v_mul_f32_e32 v34, v141, v34
	v_mul_f32_e32 v35, v141, v35
	v_mul_f32_e32 v36, v141, v36
	v_mul_f32_e32 v22, v22, v33
	v_mul_f32_e32 v23, v23, v35
	v_mul_f32_e32 v18, v18, v34
	v_mul_f32_e32 v19, v19, v36
	v_cvt_pk_fp8_f32 v30, v22, v23
	v_cvt_pk_fp8_f32 v31, v18, v19
	v_cvt_f32_ubyte2_e32 v37, v184
	v_cvt_f32_ubyte2_e32 v38, v185
	v_cvt_f32_ubyte3_e32 v26, v184
	v_cvt_f32_ubyte3_e32 v27, v185
	v_mul_f32_e32 v37, v141, v37
	v_mul_f32_e32 v38, v141, v38
	v_mul_f32_e32 v26, v141, v26
	v_mul_f32_e32 v27, v141, v27
	v_mul_f32_e32 v24, v24, v37
	v_mul_f32_e32 v25, v25, v26
	v_mul_f32_e32 v18, v20, v38
	v_mul_f32_e32 v19, v21, v27
	v_cvt_pk_fp8_f32 v30, v24, v25 op_sel:[0,0,1]
	v_cvt_pk_fp8_f32 v31, v18, v19 op_sel:[0,0,1]
	v_ashrrev_i32_e32 v33, 31, v32
	v_lshl_add_u64 v[18:19], v[32:33], 3, s[16:17]
	v_lshl_add_u64 v[18:19], v[18:19], 0, s[6:7]
	global_store_dwordx2 v[28:29], v[30:31], off offset:128
	v_mov_b32_e32 v20, 0
	v_mov_b32_e32 v21, 0
	v_add_u32_e32 v22, 0xb0, v134
	v_ashrrev_i32_e32 v23, 31, v22
	v_add_u32_e32 v24, 0x3c0, v130
	v_lshlrev_b64 v[22:23], 11, v[22:23]
	v_ashrrev_i32_e32 v25, 31, v24
	v_lshl_add_u64 v[22:23], s[18:19], 0, v[22:23]
	s_waitcnt vmcnt(15)
	v_cvt_f32_ubyte0_e32 v26, v186
	v_cvt_f32_ubyte0_e32 v27, v187
	v_cvt_f32_ubyte1_e32 v28, v186
	v_cvt_f32_ubyte1_e32 v29, v187
	v_mul_f32_e32 v26, v141, v26
	v_mul_f32_e32 v27, v141, v27
	v_mul_f32_e32 v28, v141, v28
	v_mul_f32_e32 v29, v141, v29
	v_mul_f32_e32 v14, v14, v26
	v_mul_f32_e32 v15, v15, v28
	v_mul_f32_e32 v10, v10, v27
	v_mul_f32_e32 v11, v11, v29
	v_cvt_pk_fp8_f32 v20, v14, v15
	v_cvt_pk_fp8_f32 v21, v10, v11
	v_cvt_f32_ubyte2_e32 v30, v186
	v_cvt_f32_ubyte2_e32 v31, v187
	v_cvt_f32_ubyte3_e32 v18, v186
	v_cvt_f32_ubyte3_e32 v19, v187
	v_mul_f32_e32 v30, v141, v30
	v_mul_f32_e32 v31, v141, v31
	v_mul_f32_e32 v18, v141, v18
	v_mul_f32_e32 v19, v141, v19
	v_mul_f32_e32 v16, v16, v30
	v_mul_f32_e32 v17, v17, v18
	v_mul_f32_e32 v10, v12, v31
	v_mul_f32_e32 v11, v13, v19
	v_cvt_pk_fp8_f32 v20, v16, v17 op_sel:[0,0,1]
	v_cvt_pk_fp8_f32 v21, v10, v11 op_sel:[0,0,1]
	v_lshl_add_u64 v[10:11], v[24:25], 3, s[16:17]
	v_lshl_add_u64 v[12:13], v[22:23], 0, v[132:133]
	v_lshl_add_u64 v[10:11], v[10:11], 0, s[6:7]
	global_store_dwordx2 v[12:13], v[20:21], off
	v_mov_b32_e32 v14, 0
	v_mov_b32_e32 v15, 0
	s_mov_b64 s[6:7], -1
	s_waitcnt vmcnt(15)
	v_cvt_f32_ubyte0_e32 v16, v188
	v_cvt_f32_ubyte0_e32 v17, v189
	v_cvt_f32_ubyte1_e32 v18, v188
	v_cvt_f32_ubyte1_e32 v19, v189
	v_mul_f32_e32 v16, v141, v16
	v_mul_f32_e32 v17, v141, v17
	v_mul_f32_e32 v18, v141, v18
	v_mul_f32_e32 v19, v141, v19
	v_mul_f32_e32 v6, v6, v16
	v_mul_f32_e32 v7, v7, v18
	v_mul_f32_e32 v2, v2, v17
	v_mul_f32_e32 v3, v3, v19
	v_cvt_pk_fp8_f32 v14, v6, v7
	v_cvt_pk_fp8_f32 v15, v2, v3
	v_cvt_f32_ubyte2_e32 v20, v188
	v_cvt_f32_ubyte2_e32 v21, v189
	v_cvt_f32_ubyte3_e32 v10, v188
	v_cvt_f32_ubyte3_e32 v11, v189
	v_mul_f32_e32 v20, v141, v20
	v_mul_f32_e32 v21, v141, v21
	v_mul_f32_e32 v10, v141, v10
	v_mul_f32_e32 v11, v141, v11
	v_mul_f32_e32 v8, v8, v20
	v_mul_f32_e32 v9, v9, v10
	v_mul_f32_e32 v2, v4, v21
	v_mul_f32_e32 v3, v5, v11
	v_cvt_pk_fp8_f32 v14, v8, v9 op_sel:[0,0,1]
	v_cvt_pk_fp8_f32 v15, v2, v3 op_sel:[0,0,1]
	global_store_dwordx2 v[12:13], v[14:15], off offset:128
	s_cbranch_vccnz .LBB0_3028
	s_andn2_b64 vcc, exec, s[14:15]
	s_cbranch_vccnz .LBB0_3027
	s_barrier
	s_branch .LBB0_3027
